# cache policy: P0 loads of the once-read f32 activations (x and mem rows) made non-temporal
# speedup vs baseline: 1.0110x; 1.0110x over previous
; __device__ __forceinline__ unsigned pk2(float lo, float hi) { return f2bf(lo) | (f2bf(hi) << 16); }
; __device__ __forceinline__ void row_item(const float* x, bf16_t* xb, float* ss, int r, int lane) {
;     const f32x4* xr = (const f32x4*)(x + (size_t)r * DM) + lane; u32x2* o = (u32x2*)(xb + (size_t)r * DM) + lane; float s = 0.f;
;     f32x4 v[16];
; #pragma unroll
;     for (int j = 0; j < 16; ++j) v[j] = xr[64 * j];
;     asm volatile("" ::: "memory");
; #pragma unroll
;     for (int j = 0; j < 16; ++j) { s += (v[j][0] * v[j][0] + v[j][1] * v[j][1]) + (v[j][2] * v[j][2] + v[j][3] * v[j][3]); u32x2 w; w.x = pk2(v[j][0], v[j][1]); w.y = pk2(v[j][2], v[j][3]); o[64 * j] = w; }
.LBB0_50:
	v_add_co_u32_e32 v18, vcc, 0xffffd000, v30
	v_lshl_add_u64 v[20:21], s[8:9], 0, v[28:29]
	s_nop 0
	v_addc_co_u32_e32 v19, vcc, -1, v31, vcc
	global_load_dwordx4 v[44:47], v[18:19], off offset:-3072 nt
	global_load_dwordx4 v[48:51], v[18:19], off offset:-2048 nt
	global_load_dwordx4 v[52:55], v[18:19], off offset:-1024 nt
	global_load_dwordx4 v[14:17], v[30:31], off offset:-3072 nt
	global_load_dwordx4 v[10:13], v[30:31], off offset:-2048 nt
	global_load_dwordx4 v[6:9], v[30:31], off offset:-1024 nt
	s_waitcnt lgkmcnt(0)
	global_load_dwordx4 v[2:5], v[30:31], off nt
	global_load_dwordx4 v[56:59], v[18:19], off nt
	v_add_co_u32_e32 v22, vcc, 0xffffe000, v30
	v_add_co_u32_e64 v84, s[6:7], s20, v20
	s_nop 0
	v_addc_co_u32_e32 v23, vcc, -1, v31, vcc
	global_load_dwordx4 v[60:63], v[22:23], off offset:-3072 nt
	global_load_dwordx4 v[64:67], v[22:23], off offset:-2048 nt
	global_load_dwordx4 v[68:71], v[22:23], off offset:-1024 nt
	global_load_dwordx4 v[72:75], v[22:23], off nt
	v_addc_co_u32_e64 v85, s[6:7], 0, v21, s[6:7]
	v_add_co_u32_e32 v18, vcc, 0xfffff000, v30
	v_add_co_u32_e64 v32, s[6:7], s21, v20
	s_nop 0
	v_addc_co_u32_e32 v19, vcc, -1, v31, vcc
	v_addc_co_u32_e64 v33, s[6:7], 0, v21, s[6:7]
	global_load_dwordx4 v[76:79], v[18:19], off offset:-3072 nt
	global_load_dwordx4 v[80:83], v[18:19], off offset:-2048 nt
	global_load_dwordx4 v[22:25], v[18:19], off offset:-1024 nt
	s_nop 0
	global_load_dwordx4 v[18:21], v[30:31], off offset:-4096 nt
	v_cmp_lt_i32_e32 vcc, v36, v35
	s_waitcnt vmcnt(15)
	v_mul_f32_e32 v43, v45, v45
	v_mul_f32_e32 v86, v47, v47
	v_and_b32_sdwa v89, v47, v42 dst_sel:DWORD dst_unused:UNUSED_PAD src0_sel:WORD_1 src1_sel:DWORD
	v_and_b32_sdwa v90, v45, v42 dst_sel:DWORD dst_unused:UNUSED_PAD src0_sel:WORD_1 src1_sel:DWORD
	s_waitcnt vmcnt(14)
	v_and_b32_sdwa v96, v49, v42 dst_sel:DWORD dst_unused:UNUSED_PAD src0_sel:WORD_1 src1_sel:DWORD
	v_and_b32_sdwa v87, v46, v42 dst_sel:DWORD dst_unused:UNUSED_PAD src0_sel:WORD_1 src1_sel:DWORD
	v_and_b32_sdwa v88, v44, v42 dst_sel:DWORD dst_unused:UNUSED_PAD src0_sel:WORD_1 src1_sel:DWORD
	v_mul_f32_e32 v91, v49, v49
	v_and_b32_sdwa v94, v48, v42 dst_sel:DWORD dst_unused:UNUSED_PAD src0_sel:WORD_1 src1_sel:DWORD
	v_and_b32_sdwa v95, v51, v42 dst_sel:DWORD dst_unused:UNUSED_PAD src0_sel:WORD_1 src1_sel:DWORD
	v_fmac_f32_e32 v43, v44, v44
	v_fmac_f32_e32 v86, v46, v46
	v_add3_u32 v47, v47, v89, s11
	v_add3_u32 v45, v45, v90, s11
	v_add3_u32 v49, v49, v96, s11
	v_mul_f32_e32 v92, v51, v51
	v_and_b32_sdwa v93, v50, v42 dst_sel:DWORD dst_unused:UNUSED_PAD src0_sel:WORD_1 src1_sel:DWORD
	v_add3_u32 v44, v44, v88, s11
	v_add3_u32 v46, v46, v87, s11
	v_fmac_f32_e32 v91, v48, v48
	v_add3_u32 v48, v48, v94, s11
	v_add3_u32 v51, v51, v95, s11
	v_add_f32_e32 v43, v43, v86
	v_and_b32_e32 v47, 0xffff0000, v47
	v_and_b32_e32 v86, 0xffff0000, v45
	v_and_b32_e32 v49, 0xffff0000, v49
	v_fmac_f32_e32 v92, v50, v50
	v_add3_u32 v50, v50, v93, s11
	v_and_b32_e32 v51, 0xffff0000, v51
	v_or_b32_sdwa v45, v47, v46 dst_sel:DWORD dst_unused:UNUSED_PAD src0_sel:DWORD src1_sel:WORD_1
	v_or_b32_sdwa v44, v86, v44 dst_sel:DWORD dst_unused:UNUSED_PAD src0_sel:DWORD src1_sel:WORD_1
	v_or_b32_sdwa v46, v49, v48 dst_sel:DWORD dst_unused:UNUSED_PAD src0_sel:DWORD src1_sel:WORD_1
	v_or_b32_sdwa v47, v51, v50 dst_sel:DWORD dst_unused:UNUSED_PAD src0_sel:DWORD src1_sel:WORD_1
	global_store_dwordx2 v[32:33], v[44:45], off offset:-4096
	global_store_dwordx2 v[84:85], v[46:47], off offset:512
	s_waitcnt vmcnt(15)
	v_and_b32_sdwa v45, v55, v42 dst_sel:DWORD dst_unused:UNUSED_PAD src0_sel:WORD_1 src1_sel:DWORD
	v_and_b32_sdwa v46, v53, v42 dst_sel:DWORD dst_unused:UNUSED_PAD src0_sel:WORD_1 src1_sel:DWORD
	v_mul_f32_e32 v97, v53, v53
	v_and_b32_sdwa v99, v54, v42 dst_sel:DWORD dst_unused:UNUSED_PAD src0_sel:WORD_1 src1_sel:DWORD
	v_and_b32_sdwa v100, v52, v42 dst_sel:DWORD dst_unused:UNUSED_PAD src0_sel:WORD_1 src1_sel:DWORD
	v_add3_u32 v45, v55, v45, s11
	v_add3_u32 v46, v53, v46, s11
	v_fmac_f32_e32 v97, v52, v52
	v_add3_u32 v52, v52, v100, s11
	v_add3_u32 v44, v54, v99, s11
	v_and_b32_e32 v45, 0xffff0000, v45
	v_and_b32_e32 v46, 0xffff0000, v46
	v_or_b32_sdwa v45, v45, v44 dst_sel:DWORD dst_unused:UNUSED_PAD src0_sel:DWORD src1_sel:WORD_1
	v_or_b32_sdwa v44, v46, v52 dst_sel:DWORD dst_unused:UNUSED_PAD src0_sel:DWORD src1_sel:WORD_1
	v_mul_f32_e32 v98, v55, v55
	global_store_dwordx2 v[84:85], v[44:45], off offset:1024
	s_waitcnt vmcnt(11)
	v_mul_f32_e32 v44, v57, v57
	v_mul_f32_e32 v45, v59, v59
	v_fmac_f32_e32 v98, v54, v54
	v_add_f32_e32 v87, v91, v92
	v_fmac_f32_e32 v44, v56, v56
	v_fmac_f32_e32 v45, v58, v58
	v_add_f32_e32 v88, v97, v98
	v_add_f32_e32 v43, v43, v87
	v_add_f32_e32 v44, v44, v45
	v_and_b32_sdwa v45, v56, v42 dst_sel:DWORD dst_unused:UNUSED_PAD src0_sel:WORD_1 src1_sel:DWORD
	v_add_f32_e32 v43, v43, v88
	v_add3_u32 v46, v56, v45, s11
	v_and_b32_sdwa v45, v59, v42 dst_sel:DWORD dst_unused:UNUSED_PAD src0_sel:WORD_1 src1_sel:DWORD
	v_and_b32_sdwa v47, v57, v42 dst_sel:DWORD dst_unused:UNUSED_PAD src0_sel:WORD_1 src1_sel:DWORD
	v_add_f32_e32 v43, v43, v44
	v_and_b32_sdwa v44, v58, v42 dst_sel:DWORD dst_unused:UNUSED_PAD src0_sel:WORD_1 src1_sel:DWORD
	v_add3_u32 v45, v59, v45, s11
	v_add3_u32 v47, v57, v47, s11
	v_add3_u32 v44, v58, v44, s11
	v_and_b32_e32 v45, 0xffff0000, v45
	v_and_b32_e32 v47, 0xffff0000, v47
	v_or_b32_sdwa v45, v45, v44 dst_sel:DWORD dst_unused:UNUSED_PAD src0_sel:DWORD src1_sel:WORD_1
	v_or_b32_sdwa v44, v47, v46 dst_sel:DWORD dst_unused:UNUSED_PAD src0_sel:DWORD src1_sel:WORD_1
	global_store_dwordx2 v[84:85], v[44:45], off offset:1536
	s_waitcnt vmcnt(11)
; __device__ __forceinline__ unsigned pk2(float lo, float hi) { return f2bf(lo) | (f2bf(hi) << 16); }
; __device__ __forceinline__ void row_item(const float* x, bf16_t* xb, float* ss, int r, int lane) {
;     ...
;     for (int j = 0; j < 16; ++j) { s += (v[j][0] * v[j][0] + v[j][1] * v[j][1]) + (v[j][2] * v[j][2] + v[j][3] * v[j][3]); u32x2 w; w.x = pk2(v[j][0], v[j][1]); w.y = pk2(v[j][2], v[j][3]); o[64 * j] = w; }
	v_mul_f32_e32 v44, v61, v61
	v_mul_f32_e32 v45, v63, v63
	v_fmac_f32_e32 v44, v60, v60
	v_fmac_f32_e32 v45, v62, v62
	v_add_f32_e32 v44, v44, v45
	v_and_b32_sdwa v45, v60, v42 dst_sel:DWORD dst_unused:UNUSED_PAD src0_sel:WORD_1 src1_sel:DWORD
	v_add3_u32 v46, v60, v45, s11
	v_and_b32_sdwa v45, v63, v42 dst_sel:DWORD dst_unused:UNUSED_PAD src0_sel:WORD_1 src1_sel:DWORD
	v_and_b32_sdwa v47, v61, v42 dst_sel:DWORD dst_unused:UNUSED_PAD src0_sel:WORD_1 src1_sel:DWORD
	v_add_f32_e32 v43, v43, v44
	v_and_b32_sdwa v44, v62, v42 dst_sel:DWORD dst_unused:UNUSED_PAD src0_sel:WORD_1 src1_sel:DWORD
	v_add3_u32 v45, v63, v45, s11
	v_add3_u32 v47, v61, v47, s11
	v_add3_u32 v44, v62, v44, s11
	v_and_b32_e32 v45, 0xffff0000, v45
	v_and_b32_e32 v47, 0xffff0000, v47
	v_or_b32_sdwa v45, v45, v44 dst_sel:DWORD dst_unused:UNUSED_PAD src0_sel:DWORD src1_sel:WORD_1
	v_or_b32_sdwa v44, v47, v46 dst_sel:DWORD dst_unused:UNUSED_PAD src0_sel:DWORD src1_sel:WORD_1
	global_store_dwordx2 v[84:85], v[44:45], off offset:2048
	s_waitcnt vmcnt(11)
	v_mul_f32_e32 v44, v65, v65
	v_mul_f32_e32 v45, v67, v67
	v_fmac_f32_e32 v44, v64, v64
	v_fmac_f32_e32 v45, v66, v66
	v_add_f32_e32 v44, v44, v45
	v_and_b32_sdwa v45, v64, v42 dst_sel:DWORD dst_unused:UNUSED_PAD src0_sel:WORD_1 src1_sel:DWORD
	v_add3_u32 v46, v64, v45, s11
	v_and_b32_sdwa v45, v67, v42 dst_sel:DWORD dst_unused:UNUSED_PAD src0_sel:WORD_1 src1_sel:DWORD
	v_and_b32_sdwa v47, v65, v42 dst_sel:DWORD dst_unused:UNUSED_PAD src0_sel:WORD_1 src1_sel:DWORD
	v_add_f32_e32 v43, v43, v44
	v_and_b32_sdwa v44, v66, v42 dst_sel:DWORD dst_unused:UNUSED_PAD src0_sel:WORD_1 src1_sel:DWORD
	v_add3_u32 v45, v67, v45, s11
	v_add3_u32 v47, v65, v47, s11
	v_add3_u32 v44, v66, v44, s11
	v_and_b32_e32 v45, 0xffff0000, v45
	v_and_b32_e32 v47, 0xffff0000, v47
	v_or_b32_sdwa v45, v45, v44 dst_sel:DWORD dst_unused:UNUSED_PAD src0_sel:DWORD src1_sel:WORD_1
	v_or_b32_sdwa v44, v47, v46 dst_sel:DWORD dst_unused:UNUSED_PAD src0_sel:DWORD src1_sel:WORD_1
	global_store_dwordx2 v[84:85], v[44:45], off offset:2560
	s_waitcnt vmcnt(11)
	v_mul_f32_e32 v44, v69, v69
	v_mul_f32_e32 v45, v71, v71
	v_fmac_f32_e32 v44, v68, v68
	v_fmac_f32_e32 v45, v70, v70
	v_add_f32_e32 v44, v44, v45
	v_and_b32_sdwa v45, v68, v42 dst_sel:DWORD dst_unused:UNUSED_PAD src0_sel:WORD_1 src1_sel:DWORD
	v_add3_u32 v46, v68, v45, s11
	v_and_b32_sdwa v45, v71, v42 dst_sel:DWORD dst_unused:UNUSED_PAD src0_sel:WORD_1 src1_sel:DWORD
	v_and_b32_sdwa v47, v69, v42 dst_sel:DWORD dst_unused:UNUSED_PAD src0_sel:WORD_1 src1_sel:DWORD
	v_add_f32_e32 v43, v43, v44
	v_and_b32_sdwa v44, v70, v42 dst_sel:DWORD dst_unused:UNUSED_PAD src0_sel:WORD_1 src1_sel:DWORD
	v_add3_u32 v45, v71, v45, s11
	v_add3_u32 v47, v69, v47, s11
	v_add3_u32 v44, v70, v44, s11
	v_and_b32_e32 v45, 0xffff0000, v45
	v_and_b32_e32 v47, 0xffff0000, v47
	v_or_b32_sdwa v45, v45, v44 dst_sel:DWORD dst_unused:UNUSED_PAD src0_sel:DWORD src1_sel:WORD_1
	v_or_b32_sdwa v44, v47, v46 dst_sel:DWORD dst_unused:UNUSED_PAD src0_sel:DWORD src1_sel:WORD_1
	global_store_dwordx2 v[84:85], v[44:45], off offset:3072
	s_waitcnt vmcnt(11)
	v_mul_f32_e32 v44, v73, v73
	v_mul_f32_e32 v45, v75, v75
	v_fmac_f32_e32 v44, v72, v72
	v_fmac_f32_e32 v45, v74, v74
	v_add_f32_e32 v44, v44, v45
	v_and_b32_sdwa v45, v72, v42 dst_sel:DWORD dst_unused:UNUSED_PAD src0_sel:WORD_1 src1_sel:DWORD
	v_add3_u32 v46, v72, v45, s11
	v_and_b32_sdwa v45, v75, v42 dst_sel:DWORD dst_unused:UNUSED_PAD src0_sel:WORD_1 src1_sel:DWORD
	v_and_b32_sdwa v47, v73, v42 dst_sel:DWORD dst_unused:UNUSED_PAD src0_sel:WORD_1 src1_sel:DWORD
	v_add_f32_e32 v43, v43, v44
	v_and_b32_sdwa v44, v74, v42 dst_sel:DWORD dst_unused:UNUSED_PAD src0_sel:WORD_1 src1_sel:DWORD
	v_add3_u32 v45, v75, v45, s11
	v_add3_u32 v47, v73, v47, s11
	v_add3_u32 v44, v74, v44, s11
	v_and_b32_e32 v45, 0xffff0000, v45
	v_and_b32_e32 v47, 0xffff0000, v47
	v_or_b32_sdwa v45, v45, v44 dst_sel:DWORD dst_unused:UNUSED_PAD src0_sel:DWORD src1_sel:WORD_1
	v_or_b32_sdwa v44, v47, v46 dst_sel:DWORD dst_unused:UNUSED_PAD src0_sel:DWORD src1_sel:WORD_1
	global_store_dwordx2 v[84:85], v[44:45], off offset:3584
	s_waitcnt vmcnt(11)
	v_mul_f32_e32 v44, v77, v77
	v_mul_f32_e32 v45, v79, v79
	v_fmac_f32_e32 v44, v76, v76
	v_fmac_f32_e32 v45, v78, v78
	v_add_f32_e32 v44, v44, v45
	v_and_b32_sdwa v45, v76, v42 dst_sel:DWORD dst_unused:UNUSED_PAD src0_sel:WORD_1 src1_sel:DWORD
	v_add3_u32 v46, v76, v45, s11
	v_and_b32_sdwa v45, v79, v42 dst_sel:DWORD dst_unused:UNUSED_PAD src0_sel:WORD_1 src1_sel:DWORD
	v_and_b32_sdwa v47, v77, v42 dst_sel:DWORD dst_unused:UNUSED_PAD src0_sel:WORD_1 src1_sel:DWORD
	v_add_f32_e32 v43, v43, v44
	v_and_b32_sdwa v44, v78, v42 dst_sel:DWORD dst_unused:UNUSED_PAD src0_sel:WORD_1 src1_sel:DWORD
	v_add3_u32 v45, v79, v45, s11
	v_add3_u32 v47, v77, v47, s11
	v_add3_u32 v44, v78, v44, s11
	v_and_b32_e32 v45, 0xffff0000, v45
	v_and_b32_e32 v47, 0xffff0000, v47
	v_or_b32_sdwa v45, v45, v44 dst_sel:DWORD dst_unused:UNUSED_PAD src0_sel:DWORD src1_sel:WORD_1
	v_or_b32_sdwa v44, v47, v46 dst_sel:DWORD dst_unused:UNUSED_PAD src0_sel:DWORD src1_sel:WORD_1
	global_store_dwordx2 v[32:33], v[44:45], off
	s_waitcnt vmcnt(11)
; __device__ __forceinline__ unsigned pk2(float lo, float hi) { return f2bf(lo) | (f2bf(hi) << 16); }
; __device__ __forceinline__ float wave_sum(float v) {
; #pragma unroll
;     for (int o = 1; o < 64; o <<= 1) v += __shfl_xor(v, o);
;     return v;
; __device__ __forceinline__ void row_item(const float* x, bf16_t* xb, float* ss, int r, int lane) {
;     ...
;     for (int j = 0; j < 16; ++j) { s += (v[j][0] * v[j][0] + v[j][1] * v[j][1]) + (v[j][2] * v[j][2] + v[j][3] * v[j][3]); u32x2 w; w.x = pk2(v[j][0], v[j][1]); w.y = pk2(v[j][2], v[j][3]); o[64 * j] = w; }
;     s = wave_sum(s); if (lane == 0) ss[r] = s;
	v_mul_f32_e32 v44, v81, v81
	v_mul_f32_e32 v45, v83, v83
	v_fmac_f32_e32 v44, v80, v80
	v_fmac_f32_e32 v45, v82, v82
	v_add_f32_e32 v44, v44, v45
	v_and_b32_sdwa v45, v80, v42 dst_sel:DWORD dst_unused:UNUSED_PAD src0_sel:WORD_1 src1_sel:DWORD
	v_add3_u32 v46, v80, v45, s11
	v_and_b32_sdwa v45, v83, v42 dst_sel:DWORD dst_unused:UNUSED_PAD src0_sel:WORD_1 src1_sel:DWORD
	v_and_b32_sdwa v47, v81, v42 dst_sel:DWORD dst_unused:UNUSED_PAD src0_sel:WORD_1 src1_sel:DWORD
	v_add_f32_e32 v43, v43, v44
	v_and_b32_sdwa v44, v82, v42 dst_sel:DWORD dst_unused:UNUSED_PAD src0_sel:WORD_1 src1_sel:DWORD
	v_add3_u32 v45, v83, v45, s11
	v_add3_u32 v47, v81, v47, s11
	v_add3_u32 v44, v82, v44, s11
	v_and_b32_e32 v45, 0xffff0000, v45
	v_and_b32_e32 v47, 0xffff0000, v47
	v_or_b32_sdwa v45, v45, v44 dst_sel:DWORD dst_unused:UNUSED_PAD src0_sel:DWORD src1_sel:WORD_1
	v_or_b32_sdwa v44, v47, v46 dst_sel:DWORD dst_unused:UNUSED_PAD src0_sel:DWORD src1_sel:WORD_1
	global_store_dwordx2 v[32:33], v[44:45], off offset:512
	s_waitcnt vmcnt(11)
	v_mul_f32_e32 v44, v23, v23
	v_mul_f32_e32 v45, v25, v25
	v_fmac_f32_e32 v44, v22, v22
	v_fmac_f32_e32 v45, v24, v24
	v_add_f32_e32 v44, v44, v45
	v_add_f32_e32 v43, v43, v44
	v_and_b32_sdwa v44, v24, v42 dst_sel:DWORD dst_unused:UNUSED_PAD src0_sel:WORD_1 src1_sel:DWORD
	v_and_b32_sdwa v45, v22, v42 dst_sel:DWORD dst_unused:UNUSED_PAD src0_sel:WORD_1 src1_sel:DWORD
	v_add3_u32 v22, v22, v45, s11
	v_add3_u32 v24, v24, v44, s11
	v_and_b32_sdwa v44, v25, v42 dst_sel:DWORD dst_unused:UNUSED_PAD src0_sel:WORD_1 src1_sel:DWORD
	v_and_b32_sdwa v45, v23, v42 dst_sel:DWORD dst_unused:UNUSED_PAD src0_sel:WORD_1 src1_sel:DWORD
	v_add3_u32 v25, v25, v44, s11
	v_add3_u32 v23, v23, v45, s11
	v_and_b32_e32 v25, 0xffff0000, v25
	v_and_b32_e32 v44, 0xffff0000, v23
	v_or_b32_sdwa v23, v25, v24 dst_sel:DWORD dst_unused:UNUSED_PAD src0_sel:DWORD src1_sel:WORD_1
	v_or_b32_sdwa v22, v44, v22 dst_sel:DWORD dst_unused:UNUSED_PAD src0_sel:DWORD src1_sel:WORD_1
	global_store_dwordx2 v[32:33], v[22:23], off offset:1024
	s_waitcnt vmcnt(11)
	v_mul_f32_e32 v22, v19, v19
	v_mul_f32_e32 v23, v21, v21
	v_fmac_f32_e32 v22, v18, v18
	v_fmac_f32_e32 v23, v20, v20
	v_add_f32_e32 v22, v22, v23
	v_and_b32_sdwa v23, v20, v42 dst_sel:DWORD dst_unused:UNUSED_PAD src0_sel:WORD_1 src1_sel:DWORD
	v_and_b32_sdwa v24, v18, v42 dst_sel:DWORD dst_unused:UNUSED_PAD src0_sel:WORD_1 src1_sel:DWORD
	v_add3_u32 v18, v18, v24, s11
	v_add3_u32 v20, v20, v23, s11
	v_and_b32_sdwa v23, v21, v42 dst_sel:DWORD dst_unused:UNUSED_PAD src0_sel:WORD_1 src1_sel:DWORD
	v_and_b32_sdwa v24, v19, v42 dst_sel:DWORD dst_unused:UNUSED_PAD src0_sel:WORD_1 src1_sel:DWORD
	v_add3_u32 v21, v21, v23, s11
	v_add3_u32 v19, v19, v24, s11
	v_and_b32_e32 v21, 0xffff0000, v21
	v_and_b32_e32 v23, 0xffff0000, v19
	v_or_b32_sdwa v19, v21, v20 dst_sel:DWORD dst_unused:UNUSED_PAD src0_sel:DWORD src1_sel:WORD_1
	v_or_b32_sdwa v18, v23, v18 dst_sel:DWORD dst_unused:UNUSED_PAD src0_sel:DWORD src1_sel:WORD_1
	global_store_dwordx2 v[32:33], v[18:19], off offset:1536
	v_mul_f32_e32 v18, v15, v15
	v_mul_f32_e32 v19, v17, v17
	v_fmac_f32_e32 v18, v14, v14
	v_fmac_f32_e32 v19, v16, v16
	v_add_f32_e32 v18, v18, v19
	v_and_b32_sdwa v19, v16, v42 dst_sel:DWORD dst_unused:UNUSED_PAD src0_sel:WORD_1 src1_sel:DWORD
	v_and_b32_sdwa v20, v14, v42 dst_sel:DWORD dst_unused:UNUSED_PAD src0_sel:WORD_1 src1_sel:DWORD
	v_add3_u32 v14, v14, v20, s11
	v_add3_u32 v16, v16, v19, s11
	v_and_b32_sdwa v19, v17, v42 dst_sel:DWORD dst_unused:UNUSED_PAD src0_sel:WORD_1 src1_sel:DWORD
	v_and_b32_sdwa v20, v15, v42 dst_sel:DWORD dst_unused:UNUSED_PAD src0_sel:WORD_1 src1_sel:DWORD
	v_add3_u32 v17, v17, v19, s11
	v_add3_u32 v15, v15, v20, s11
	v_and_b32_e32 v17, 0xffff0000, v17
	v_and_b32_e32 v19, 0xffff0000, v15
	v_or_b32_sdwa v15, v17, v16 dst_sel:DWORD dst_unused:UNUSED_PAD src0_sel:DWORD src1_sel:WORD_1
	v_or_b32_sdwa v14, v19, v14 dst_sel:DWORD dst_unused:UNUSED_PAD src0_sel:DWORD src1_sel:WORD_1
	global_store_dwordx2 v[32:33], v[14:15], off offset:2048
	v_mul_f32_e32 v14, v11, v11
	v_mul_f32_e32 v15, v13, v13
	v_fmac_f32_e32 v14, v10, v10
	v_fmac_f32_e32 v15, v12, v12
	v_add_f32_e32 v14, v14, v15
	v_and_b32_sdwa v15, v12, v42 dst_sel:DWORD dst_unused:UNUSED_PAD src0_sel:WORD_1 src1_sel:DWORD
	v_and_b32_sdwa v16, v10, v42 dst_sel:DWORD dst_unused:UNUSED_PAD src0_sel:WORD_1 src1_sel:DWORD
	v_add3_u32 v10, v10, v16, s11
	v_add3_u32 v12, v12, v15, s11
	v_and_b32_sdwa v15, v13, v42 dst_sel:DWORD dst_unused:UNUSED_PAD src0_sel:WORD_1 src1_sel:DWORD
	v_and_b32_sdwa v16, v11, v42 dst_sel:DWORD dst_unused:UNUSED_PAD src0_sel:WORD_1 src1_sel:DWORD
	v_add3_u32 v13, v13, v15, s11
	v_add3_u32 v11, v11, v16, s11
	v_and_b32_e32 v13, 0xffff0000, v13
	v_and_b32_e32 v15, 0xffff0000, v11
	v_or_b32_sdwa v11, v13, v12 dst_sel:DWORD dst_unused:UNUSED_PAD src0_sel:DWORD src1_sel:WORD_1
	v_or_b32_sdwa v10, v15, v10 dst_sel:DWORD dst_unused:UNUSED_PAD src0_sel:DWORD src1_sel:WORD_1
	v_add_f32_e32 v22, v43, v22
	global_store_dwordx2 v[32:33], v[10:11], off offset:2560
	v_mul_f32_e32 v10, v7, v7
	v_mul_f32_e32 v11, v9, v9
	v_add_f32_e32 v18, v22, v18
	v_fmac_f32_e32 v10, v6, v6
	v_fmac_f32_e32 v11, v8, v8
	v_add_f32_e32 v14, v18, v14
	v_add_f32_e32 v10, v10, v11
	v_add_f32_e32 v10, v14, v10
	v_mul_f32_e32 v13, v3, v3
	v_mul_f32_e32 v14, v5, v5
	v_fmac_f32_e32 v13, v2, v2
	v_fmac_f32_e32 v14, v4, v4
	v_add_f32_e32 v13, v13, v14
	v_add_f32_e32 v10, v10, v13
	v_cndmask_b32_e32 v13, v34, v36, vcc
	v_lshlrev_b32_e32 v13, 2, v13
	ds_bpermute_b32 v13, v13, v10
	v_cmp_lt_i32_e32 vcc, v37, v35
	v_and_b32_sdwa v12, v6, v42 dst_sel:DWORD dst_unused:UNUSED_PAD src0_sel:WORD_1 src1_sel:DWORD
	v_and_b32_sdwa v11, v8, v42 dst_sel:DWORD dst_unused:UNUSED_PAD src0_sel:WORD_1 src1_sel:DWORD
	v_add3_u32 v6, v6, v12, s11
	s_waitcnt lgkmcnt(0)
; __device__ __forceinline__ unsigned pk2(float lo, float hi) { return f2bf(lo) | (f2bf(hi) << 16); }
; __device__ __forceinline__ float wave_sum(float v) {
; #pragma unroll
;     for (int o = 1; o < 64; o <<= 1) v += __shfl_xor(v, o);
;     return v;
; __device__ __forceinline__ void row_item(const float* x, bf16_t* xb, float* ss, int r, int lane) {
;     ...
;     for (int j = 0; j < 16; ++j) { s += (v[j][0] * v[j][0] + v[j][1] * v[j][1]) + (v[j][2] * v[j][2] + v[j][3] * v[j][3]); u32x2 w; w.x = pk2(v[j][0], v[j][1]); w.y = pk2(v[j][2], v[j][3]); o[64 * j] = w; }
;     s = wave_sum(s); if (lane == 0) ss[r] = s;
	v_add_f32_e32 v10, v10, v13
	v_cndmask_b32_e32 v13, v34, v37, vcc
	v_lshlrev_b32_e32 v13, 2, v13
	ds_bpermute_b32 v13, v13, v10
	v_and_b32_sdwa v12, v7, v42 dst_sel:DWORD dst_unused:UNUSED_PAD src0_sel:WORD_1 src1_sel:DWORD
	v_add3_u32 v8, v8, v11, s11
	v_and_b32_sdwa v11, v9, v42 dst_sel:DWORD dst_unused:UNUSED_PAD src0_sel:WORD_1 src1_sel:DWORD
	v_add3_u32 v7, v7, v12, s11
	v_cmp_lt_i32_e32 vcc, v38, v35
	v_add3_u32 v9, v9, v11, s11
	v_and_b32_e32 v11, 0xffff0000, v7
	v_cndmask_b32_e32 v7, v34, v38, vcc
	s_waitcnt lgkmcnt(0)
	v_add_f32_e32 v10, v10, v13
	v_lshlrev_b32_e32 v7, 2, v7
	ds_bpermute_b32 v12, v7, v10
	v_and_b32_e32 v9, 0xffff0000, v9
	v_cmp_lt_i32_e32 vcc, v39, v35
	v_or_b32_sdwa v7, v9, v8 dst_sel:DWORD dst_unused:UNUSED_PAD src0_sel:DWORD src1_sel:WORD_1
	v_or_b32_sdwa v6, v11, v6 dst_sel:DWORD dst_unused:UNUSED_PAD src0_sel:DWORD src1_sel:WORD_1
	v_cndmask_b32_e32 v8, v34, v39, vcc
	global_store_dwordx2 v[32:33], v[6:7], off offset:3072
	s_waitcnt lgkmcnt(0)
	v_add_f32_e32 v7, v10, v12
	v_lshlrev_b32_e32 v8, 2, v8
	ds_bpermute_b32 v8, v8, v7
	v_and_b32_sdwa v6, v4, v42 dst_sel:DWORD dst_unused:UNUSED_PAD src0_sel:WORD_1 src1_sel:DWORD
	v_cmp_lt_i32_e32 vcc, v40, v35
	v_add3_u32 v4, v4, v6, s11
	v_and_b32_sdwa v9, v2, v42 dst_sel:DWORD dst_unused:UNUSED_PAD src0_sel:WORD_1 src1_sel:DWORD
	s_waitcnt lgkmcnt(0)
	v_add_f32_e32 v6, v7, v8
	v_cndmask_b32_e32 v7, v34, v40, vcc
	v_lshlrev_b32_e32 v7, 2, v7
	ds_bpermute_b32 v7, v7, v6
	v_add3_u32 v9, v2, v9, s11
	v_and_b32_sdwa v2, v5, v42 dst_sel:DWORD dst_unused:UNUSED_PAD src0_sel:WORD_1 src1_sel:DWORD
	v_and_b32_sdwa v8, v3, v42 dst_sel:DWORD dst_unused:UNUSED_PAD src0_sel:WORD_1 src1_sel:DWORD
	v_cmp_lt_i32_e32 vcc, v41, v35
	v_add3_u32 v2, v5, v2, s11
	v_add3_u32 v5, v3, v8, s11
	v_cndmask_b32_e32 v3, v34, v41, vcc
	v_and_b32_e32 v8, 0xffff0000, v2
	s_waitcnt lgkmcnt(0)
	v_add_f32_e32 v2, v6, v7
	v_lshlrev_b32_e32 v3, 2, v3
	ds_bpermute_b32 v3, v3, v2
	v_and_b32_e32 v6, 0xffff0000, v5
	v_or_b32_sdwa v5, v8, v4 dst_sel:DWORD dst_unused:UNUSED_PAD src0_sel:DWORD src1_sel:WORD_1
	v_or_b32_sdwa v4, v6, v9 dst_sel:DWORD dst_unused:UNUSED_PAD src0_sel:DWORD src1_sel:WORD_1
	global_store_dwordx2 v[32:33], v[4:5], off offset:3584
	s_and_saveexec_b64 s[6:7], s[4:5]
	s_cbranch_execz .LBB0_49
	s_add_u32 s24, s8, s18
	s_waitcnt lgkmcnt(0)
	v_add_f32_e32 v2, v2, v3
	s_addc_u32 s25, s9, s19
	global_store_dword v27, v2, s[24:25]
	s_branch .LBB0_49

; __device__ __forceinline__ unsigned pk2(float lo, float hi) { return f2bf(lo) | (f2bf(hi) << 16); }
; __device__ __forceinline__ void row_item(const float* x, bf16_t* xb, float* ss, int r, int lane) {
;     const f32x4* xr = (const f32x4*)(x + (size_t)r * DM) + lane; u32x2* o = (u32x2*)(xb + (size_t)r * DM) + lane; float s = 0.f;
;     f32x4 v[16];
; #pragma unroll
;     for (int j = 0; j < 16; ++j) v[j] = xr[64 * j];
;     asm volatile("" ::: "memory");
; #pragma unroll
;     for (int j = 0; j < 16; ++j) { s += (v[j][0] * v[j][0] + v[j][1] * v[j][1]) + (v[j][2] * v[j][2] + v[j][3] * v[j][3]); u32x2 w; w.x = pk2(v[j][0], v[j][1]); w.y = pk2(v[j][2], v[j][3]); o[64 * j] = w; }
.LBB0_55:
	v_add_co_u32_e32 v18, vcc, 0xffffd000, v30
	v_lshl_add_u64 v[20:21], s[8:9], 0, v[28:29]
	s_nop 0
	v_addc_co_u32_e32 v19, vcc, -1, v31, vcc
	global_load_dwordx4 v[42:45], v[18:19], off offset:-3072 nt
	global_load_dwordx4 v[46:49], v[18:19], off offset:-2048 nt
	global_load_dwordx4 v[50:53], v[18:19], off offset:-1024 nt
	global_load_dwordx4 v[14:17], v[30:31], off offset:-3072 nt
	global_load_dwordx4 v[10:13], v[30:31], off offset:-2048 nt
	global_load_dwordx4 v[6:9], v[30:31], off offset:-1024 nt
	s_waitcnt lgkmcnt(0)
	global_load_dwordx4 v[2:5], v[30:31], off nt
	global_load_dwordx4 v[54:57], v[18:19], off nt
	v_add_co_u32_e32 v22, vcc, 0xffffe000, v30
	v_add_co_u32_e64 v82, s[6:7], s20, v20
	s_nop 0
	v_addc_co_u32_e32 v23, vcc, -1, v31, vcc
	global_load_dwordx4 v[58:61], v[22:23], off offset:-3072 nt
	global_load_dwordx4 v[62:65], v[22:23], off offset:-2048 nt
	global_load_dwordx4 v[66:69], v[22:23], off offset:-1024 nt
	global_load_dwordx4 v[70:73], v[22:23], off nt
	v_addc_co_u32_e64 v83, s[6:7], 0, v21, s[6:7]
	v_add_co_u32_e32 v18, vcc, 0xfffff000, v30
	v_add_co_u32_e64 v32, s[6:7], s21, v20
	s_nop 0
	v_addc_co_u32_e32 v19, vcc, -1, v31, vcc
	v_addc_co_u32_e64 v33, s[6:7], 0, v21, s[6:7]
	global_load_dwordx4 v[74:77], v[18:19], off offset:-3072 nt
	global_load_dwordx4 v[78:81], v[18:19], off offset:-2048 nt
	global_load_dwordx4 v[22:25], v[18:19], off offset:-1024 nt
	s_nop 0
	global_load_dwordx4 v[18:21], v[30:31], off offset:-4096 nt
	v_cmp_lt_i32_e32 vcc, v34, v26
	s_waitcnt vmcnt(15)
	v_mul_f32_e32 v41, v43, v43
	v_mul_f32_e32 v84, v45, v45
	v_and_b32_sdwa v87, v45, v40 dst_sel:DWORD dst_unused:UNUSED_PAD src0_sel:WORD_1 src1_sel:DWORD
	v_and_b32_sdwa v88, v43, v40 dst_sel:DWORD dst_unused:UNUSED_PAD src0_sel:WORD_1 src1_sel:DWORD
	s_waitcnt vmcnt(14)
	v_and_b32_sdwa v94, v47, v40 dst_sel:DWORD dst_unused:UNUSED_PAD src0_sel:WORD_1 src1_sel:DWORD
	v_and_b32_sdwa v85, v44, v40 dst_sel:DWORD dst_unused:UNUSED_PAD src0_sel:WORD_1 src1_sel:DWORD
	v_and_b32_sdwa v86, v42, v40 dst_sel:DWORD dst_unused:UNUSED_PAD src0_sel:WORD_1 src1_sel:DWORD
	v_mul_f32_e32 v89, v47, v47
	v_and_b32_sdwa v92, v46, v40 dst_sel:DWORD dst_unused:UNUSED_PAD src0_sel:WORD_1 src1_sel:DWORD
	v_and_b32_sdwa v93, v49, v40 dst_sel:DWORD dst_unused:UNUSED_PAD src0_sel:WORD_1 src1_sel:DWORD
	v_fmac_f32_e32 v41, v42, v42
	v_fmac_f32_e32 v84, v44, v44
	v_add3_u32 v45, v45, v87, s11
	v_add3_u32 v43, v43, v88, s11
	v_add3_u32 v47, v47, v94, s11
	v_mul_f32_e32 v90, v49, v49
	v_and_b32_sdwa v91, v48, v40 dst_sel:DWORD dst_unused:UNUSED_PAD src0_sel:WORD_1 src1_sel:DWORD
	v_add3_u32 v42, v42, v86, s11
	v_add3_u32 v44, v44, v85, s11
	v_fmac_f32_e32 v89, v46, v46
	v_add3_u32 v46, v46, v92, s11
	v_add3_u32 v49, v49, v93, s11
	v_add_f32_e32 v41, v41, v84
	v_and_b32_e32 v45, 0xffff0000, v45
	v_and_b32_e32 v84, 0xffff0000, v43
	v_and_b32_e32 v47, 0xffff0000, v47
	v_fmac_f32_e32 v90, v48, v48
	v_add3_u32 v48, v48, v91, s11
	v_and_b32_e32 v49, 0xffff0000, v49
	v_or_b32_sdwa v43, v45, v44 dst_sel:DWORD dst_unused:UNUSED_PAD src0_sel:DWORD src1_sel:WORD_1
	v_or_b32_sdwa v42, v84, v42 dst_sel:DWORD dst_unused:UNUSED_PAD src0_sel:DWORD src1_sel:WORD_1
	v_or_b32_sdwa v44, v47, v46 dst_sel:DWORD dst_unused:UNUSED_PAD src0_sel:DWORD src1_sel:WORD_1
	v_or_b32_sdwa v45, v49, v48 dst_sel:DWORD dst_unused:UNUSED_PAD src0_sel:DWORD src1_sel:WORD_1
	global_store_dwordx2 v[32:33], v[42:43], off offset:-4096
	global_store_dwordx2 v[82:83], v[44:45], off offset:512
	s_waitcnt vmcnt(15)
	v_and_b32_sdwa v43, v53, v40 dst_sel:DWORD dst_unused:UNUSED_PAD src0_sel:WORD_1 src1_sel:DWORD
	v_and_b32_sdwa v44, v51, v40 dst_sel:DWORD dst_unused:UNUSED_PAD src0_sel:WORD_1 src1_sel:DWORD
	v_mul_f32_e32 v95, v51, v51
	v_and_b32_sdwa v97, v52, v40 dst_sel:DWORD dst_unused:UNUSED_PAD src0_sel:WORD_1 src1_sel:DWORD
	v_and_b32_sdwa v98, v50, v40 dst_sel:DWORD dst_unused:UNUSED_PAD src0_sel:WORD_1 src1_sel:DWORD
	v_add3_u32 v43, v53, v43, s11
	v_add3_u32 v44, v51, v44, s11
	v_fmac_f32_e32 v95, v50, v50
	v_add3_u32 v50, v50, v98, s11
	v_add3_u32 v42, v52, v97, s11
	v_and_b32_e32 v43, 0xffff0000, v43
	v_and_b32_e32 v44, 0xffff0000, v44
	v_or_b32_sdwa v43, v43, v42 dst_sel:DWORD dst_unused:UNUSED_PAD src0_sel:DWORD src1_sel:WORD_1
	v_or_b32_sdwa v42, v44, v50 dst_sel:DWORD dst_unused:UNUSED_PAD src0_sel:DWORD src1_sel:WORD_1
	v_mul_f32_e32 v96, v53, v53
	global_store_dwordx2 v[82:83], v[42:43], off offset:1024
	s_waitcnt vmcnt(11)
	v_mul_f32_e32 v42, v55, v55
	v_mul_f32_e32 v43, v57, v57
	v_fmac_f32_e32 v96, v52, v52
	v_add_f32_e32 v85, v89, v90
	v_fmac_f32_e32 v42, v54, v54
	v_fmac_f32_e32 v43, v56, v56
	v_add_f32_e32 v86, v95, v96
	v_add_f32_e32 v41, v41, v85
	v_add_f32_e32 v42, v42, v43
	v_and_b32_sdwa v43, v54, v40 dst_sel:DWORD dst_unused:UNUSED_PAD src0_sel:WORD_1 src1_sel:DWORD
	v_add_f32_e32 v41, v41, v86
	v_add3_u32 v44, v54, v43, s11
	v_and_b32_sdwa v43, v57, v40 dst_sel:DWORD dst_unused:UNUSED_PAD src0_sel:WORD_1 src1_sel:DWORD
	v_and_b32_sdwa v45, v55, v40 dst_sel:DWORD dst_unused:UNUSED_PAD src0_sel:WORD_1 src1_sel:DWORD
	v_add_f32_e32 v41, v41, v42
	v_and_b32_sdwa v42, v56, v40 dst_sel:DWORD dst_unused:UNUSED_PAD src0_sel:WORD_1 src1_sel:DWORD
	v_add3_u32 v43, v57, v43, s11
	v_add3_u32 v45, v55, v45, s11
	v_add3_u32 v42, v56, v42, s11
	v_and_b32_e32 v43, 0xffff0000, v43
	v_and_b32_e32 v45, 0xffff0000, v45
	v_or_b32_sdwa v43, v43, v42 dst_sel:DWORD dst_unused:UNUSED_PAD src0_sel:DWORD src1_sel:WORD_1
	v_or_b32_sdwa v42, v45, v44 dst_sel:DWORD dst_unused:UNUSED_PAD src0_sel:DWORD src1_sel:WORD_1
	global_store_dwordx2 v[82:83], v[42:43], off offset:1536
	s_waitcnt vmcnt(11)
; __device__ __forceinline__ unsigned pk2(float lo, float hi) { return f2bf(lo) | (f2bf(hi) << 16); }
; __device__ __forceinline__ void row_item(const float* x, bf16_t* xb, float* ss, int r, int lane) {
;     ...
;     for (int j = 0; j < 16; ++j) { s += (v[j][0] * v[j][0] + v[j][1] * v[j][1]) + (v[j][2] * v[j][2] + v[j][3] * v[j][3]); u32x2 w; w.x = pk2(v[j][0], v[j][1]); w.y = pk2(v[j][2], v[j][3]); o[64 * j] = w; }
	v_mul_f32_e32 v42, v59, v59
	v_mul_f32_e32 v43, v61, v61
	v_fmac_f32_e32 v42, v58, v58
	v_fmac_f32_e32 v43, v60, v60
	v_add_f32_e32 v42, v42, v43
	v_and_b32_sdwa v43, v58, v40 dst_sel:DWORD dst_unused:UNUSED_PAD src0_sel:WORD_1 src1_sel:DWORD
	v_add3_u32 v44, v58, v43, s11
	v_and_b32_sdwa v43, v61, v40 dst_sel:DWORD dst_unused:UNUSED_PAD src0_sel:WORD_1 src1_sel:DWORD
	v_and_b32_sdwa v45, v59, v40 dst_sel:DWORD dst_unused:UNUSED_PAD src0_sel:WORD_1 src1_sel:DWORD
	v_add_f32_e32 v41, v41, v42
	v_and_b32_sdwa v42, v60, v40 dst_sel:DWORD dst_unused:UNUSED_PAD src0_sel:WORD_1 src1_sel:DWORD
	v_add3_u32 v43, v61, v43, s11
	v_add3_u32 v45, v59, v45, s11
	v_add3_u32 v42, v60, v42, s11
	v_and_b32_e32 v43, 0xffff0000, v43
	v_and_b32_e32 v45, 0xffff0000, v45
	v_or_b32_sdwa v43, v43, v42 dst_sel:DWORD dst_unused:UNUSED_PAD src0_sel:DWORD src1_sel:WORD_1
	v_or_b32_sdwa v42, v45, v44 dst_sel:DWORD dst_unused:UNUSED_PAD src0_sel:DWORD src1_sel:WORD_1
	global_store_dwordx2 v[82:83], v[42:43], off offset:2048
	s_waitcnt vmcnt(11)
	v_mul_f32_e32 v42, v63, v63
	v_mul_f32_e32 v43, v65, v65
	v_fmac_f32_e32 v42, v62, v62
	v_fmac_f32_e32 v43, v64, v64
	v_add_f32_e32 v42, v42, v43
	v_and_b32_sdwa v43, v62, v40 dst_sel:DWORD dst_unused:UNUSED_PAD src0_sel:WORD_1 src1_sel:DWORD
	v_add3_u32 v44, v62, v43, s11
	v_and_b32_sdwa v43, v65, v40 dst_sel:DWORD dst_unused:UNUSED_PAD src0_sel:WORD_1 src1_sel:DWORD
	v_and_b32_sdwa v45, v63, v40 dst_sel:DWORD dst_unused:UNUSED_PAD src0_sel:WORD_1 src1_sel:DWORD
	v_add_f32_e32 v41, v41, v42
	v_and_b32_sdwa v42, v64, v40 dst_sel:DWORD dst_unused:UNUSED_PAD src0_sel:WORD_1 src1_sel:DWORD
	v_add3_u32 v43, v65, v43, s11
	v_add3_u32 v45, v63, v45, s11
	v_add3_u32 v42, v64, v42, s11
	v_and_b32_e32 v43, 0xffff0000, v43
	v_and_b32_e32 v45, 0xffff0000, v45
	v_or_b32_sdwa v43, v43, v42 dst_sel:DWORD dst_unused:UNUSED_PAD src0_sel:DWORD src1_sel:WORD_1
	v_or_b32_sdwa v42, v45, v44 dst_sel:DWORD dst_unused:UNUSED_PAD src0_sel:DWORD src1_sel:WORD_1
	global_store_dwordx2 v[82:83], v[42:43], off offset:2560
	s_waitcnt vmcnt(11)
	v_mul_f32_e32 v42, v67, v67
	v_mul_f32_e32 v43, v69, v69
	v_fmac_f32_e32 v42, v66, v66
	v_fmac_f32_e32 v43, v68, v68
	v_add_f32_e32 v42, v42, v43
	v_and_b32_sdwa v43, v66, v40 dst_sel:DWORD dst_unused:UNUSED_PAD src0_sel:WORD_1 src1_sel:DWORD
	v_add3_u32 v44, v66, v43, s11
	v_and_b32_sdwa v43, v69, v40 dst_sel:DWORD dst_unused:UNUSED_PAD src0_sel:WORD_1 src1_sel:DWORD
	v_and_b32_sdwa v45, v67, v40 dst_sel:DWORD dst_unused:UNUSED_PAD src0_sel:WORD_1 src1_sel:DWORD
	v_add_f32_e32 v41, v41, v42
	v_and_b32_sdwa v42, v68, v40 dst_sel:DWORD dst_unused:UNUSED_PAD src0_sel:WORD_1 src1_sel:DWORD
	v_add3_u32 v43, v69, v43, s11
	v_add3_u32 v45, v67, v45, s11
	v_add3_u32 v42, v68, v42, s11
	v_and_b32_e32 v43, 0xffff0000, v43
	v_and_b32_e32 v45, 0xffff0000, v45
	v_or_b32_sdwa v43, v43, v42 dst_sel:DWORD dst_unused:UNUSED_PAD src0_sel:DWORD src1_sel:WORD_1
	v_or_b32_sdwa v42, v45, v44 dst_sel:DWORD dst_unused:UNUSED_PAD src0_sel:DWORD src1_sel:WORD_1
	global_store_dwordx2 v[82:83], v[42:43], off offset:3072
	s_waitcnt vmcnt(11)
	v_mul_f32_e32 v42, v71, v71
	v_mul_f32_e32 v43, v73, v73
	v_fmac_f32_e32 v42, v70, v70
	v_fmac_f32_e32 v43, v72, v72
	v_add_f32_e32 v42, v42, v43
	v_and_b32_sdwa v43, v70, v40 dst_sel:DWORD dst_unused:UNUSED_PAD src0_sel:WORD_1 src1_sel:DWORD
	v_add3_u32 v44, v70, v43, s11
	v_and_b32_sdwa v43, v73, v40 dst_sel:DWORD dst_unused:UNUSED_PAD src0_sel:WORD_1 src1_sel:DWORD
	v_and_b32_sdwa v45, v71, v40 dst_sel:DWORD dst_unused:UNUSED_PAD src0_sel:WORD_1 src1_sel:DWORD
	v_add_f32_e32 v41, v41, v42
	v_and_b32_sdwa v42, v72, v40 dst_sel:DWORD dst_unused:UNUSED_PAD src0_sel:WORD_1 src1_sel:DWORD
	v_add3_u32 v43, v73, v43, s11
	v_add3_u32 v45, v71, v45, s11
	v_add3_u32 v42, v72, v42, s11
	v_and_b32_e32 v43, 0xffff0000, v43
	v_and_b32_e32 v45, 0xffff0000, v45
	v_or_b32_sdwa v43, v43, v42 dst_sel:DWORD dst_unused:UNUSED_PAD src0_sel:DWORD src1_sel:WORD_1
	v_or_b32_sdwa v42, v45, v44 dst_sel:DWORD dst_unused:UNUSED_PAD src0_sel:DWORD src1_sel:WORD_1
	global_store_dwordx2 v[82:83], v[42:43], off offset:3584
	s_waitcnt vmcnt(11)
	v_mul_f32_e32 v42, v75, v75
	v_mul_f32_e32 v43, v77, v77
	v_fmac_f32_e32 v42, v74, v74
	v_fmac_f32_e32 v43, v76, v76
	v_add_f32_e32 v42, v42, v43
	v_and_b32_sdwa v43, v74, v40 dst_sel:DWORD dst_unused:UNUSED_PAD src0_sel:WORD_1 src1_sel:DWORD
	v_add3_u32 v44, v74, v43, s11
	v_and_b32_sdwa v43, v77, v40 dst_sel:DWORD dst_unused:UNUSED_PAD src0_sel:WORD_1 src1_sel:DWORD
	v_and_b32_sdwa v45, v75, v40 dst_sel:DWORD dst_unused:UNUSED_PAD src0_sel:WORD_1 src1_sel:DWORD
	v_add_f32_e32 v41, v41, v42
	v_and_b32_sdwa v42, v76, v40 dst_sel:DWORD dst_unused:UNUSED_PAD src0_sel:WORD_1 src1_sel:DWORD
	v_add3_u32 v43, v77, v43, s11
	v_add3_u32 v45, v75, v45, s11
	v_add3_u32 v42, v76, v42, s11
	v_and_b32_e32 v43, 0xffff0000, v43
	v_and_b32_e32 v45, 0xffff0000, v45
	v_or_b32_sdwa v43, v43, v42 dst_sel:DWORD dst_unused:UNUSED_PAD src0_sel:DWORD src1_sel:WORD_1
	v_or_b32_sdwa v42, v45, v44 dst_sel:DWORD dst_unused:UNUSED_PAD src0_sel:DWORD src1_sel:WORD_1
	global_store_dwordx2 v[32:33], v[42:43], off
	s_waitcnt vmcnt(11)
; __device__ __forceinline__ unsigned pk2(float lo, float hi) { return f2bf(lo) | (f2bf(hi) << 16); }
; __device__ __forceinline__ float wave_sum(float v) {
; #pragma unroll
;     for (int o = 1; o < 64; o <<= 1) v += __shfl_xor(v, o);
;     return v;
; __device__ __forceinline__ void row_item(const float* x, bf16_t* xb, float* ss, int r, int lane) {
;     ...
;     for (int j = 0; j < 16; ++j) { s += (v[j][0] * v[j][0] + v[j][1] * v[j][1]) + (v[j][2] * v[j][2] + v[j][3] * v[j][3]); u32x2 w; w.x = pk2(v[j][0], v[j][1]); w.y = pk2(v[j][2], v[j][3]); o[64 * j] = w; }
;     s = wave_sum(s); if (lane == 0) ss[r] = s;
	v_mul_f32_e32 v42, v79, v79
	v_mul_f32_e32 v43, v81, v81
	v_fmac_f32_e32 v42, v78, v78
	v_fmac_f32_e32 v43, v80, v80
	v_add_f32_e32 v42, v42, v43
	v_and_b32_sdwa v43, v78, v40 dst_sel:DWORD dst_unused:UNUSED_PAD src0_sel:WORD_1 src1_sel:DWORD
	v_add3_u32 v44, v78, v43, s11
	v_and_b32_sdwa v43, v81, v40 dst_sel:DWORD dst_unused:UNUSED_PAD src0_sel:WORD_1 src1_sel:DWORD
	v_and_b32_sdwa v45, v79, v40 dst_sel:DWORD dst_unused:UNUSED_PAD src0_sel:WORD_1 src1_sel:DWORD
	v_add_f32_e32 v41, v41, v42
	v_and_b32_sdwa v42, v80, v40 dst_sel:DWORD dst_unused:UNUSED_PAD src0_sel:WORD_1 src1_sel:DWORD
	v_add3_u32 v43, v81, v43, s11
	v_add3_u32 v45, v79, v45, s11
	v_add3_u32 v42, v80, v42, s11
	v_and_b32_e32 v43, 0xffff0000, v43
	v_and_b32_e32 v45, 0xffff0000, v45
	v_or_b32_sdwa v43, v43, v42 dst_sel:DWORD dst_unused:UNUSED_PAD src0_sel:DWORD src1_sel:WORD_1
	v_or_b32_sdwa v42, v45, v44 dst_sel:DWORD dst_unused:UNUSED_PAD src0_sel:DWORD src1_sel:WORD_1
	global_store_dwordx2 v[32:33], v[42:43], off offset:512
	s_waitcnt vmcnt(11)
	v_mul_f32_e32 v42, v23, v23
	v_mul_f32_e32 v43, v25, v25
	v_fmac_f32_e32 v42, v22, v22
	v_fmac_f32_e32 v43, v24, v24
	v_add_f32_e32 v42, v42, v43
	v_add_f32_e32 v41, v41, v42
	v_and_b32_sdwa v42, v24, v40 dst_sel:DWORD dst_unused:UNUSED_PAD src0_sel:WORD_1 src1_sel:DWORD
	v_and_b32_sdwa v43, v22, v40 dst_sel:DWORD dst_unused:UNUSED_PAD src0_sel:WORD_1 src1_sel:DWORD
	v_add3_u32 v22, v22, v43, s11
	v_add3_u32 v24, v24, v42, s11
	v_and_b32_sdwa v42, v25, v40 dst_sel:DWORD dst_unused:UNUSED_PAD src0_sel:WORD_1 src1_sel:DWORD
	v_and_b32_sdwa v43, v23, v40 dst_sel:DWORD dst_unused:UNUSED_PAD src0_sel:WORD_1 src1_sel:DWORD
	v_add3_u32 v25, v25, v42, s11
	v_add3_u32 v23, v23, v43, s11
	v_and_b32_e32 v25, 0xffff0000, v25
	v_and_b32_e32 v42, 0xffff0000, v23
	v_or_b32_sdwa v23, v25, v24 dst_sel:DWORD dst_unused:UNUSED_PAD src0_sel:DWORD src1_sel:WORD_1
	v_or_b32_sdwa v22, v42, v22 dst_sel:DWORD dst_unused:UNUSED_PAD src0_sel:DWORD src1_sel:WORD_1
	global_store_dwordx2 v[32:33], v[22:23], off offset:1024
	s_waitcnt vmcnt(11)
	v_mul_f32_e32 v22, v19, v19
	v_mul_f32_e32 v23, v21, v21
	v_fmac_f32_e32 v22, v18, v18
	v_fmac_f32_e32 v23, v20, v20
	v_add_f32_e32 v22, v22, v23
	v_and_b32_sdwa v23, v20, v40 dst_sel:DWORD dst_unused:UNUSED_PAD src0_sel:WORD_1 src1_sel:DWORD
	v_and_b32_sdwa v24, v18, v40 dst_sel:DWORD dst_unused:UNUSED_PAD src0_sel:WORD_1 src1_sel:DWORD
	v_add3_u32 v18, v18, v24, s11
	v_add3_u32 v20, v20, v23, s11
	v_and_b32_sdwa v23, v21, v40 dst_sel:DWORD dst_unused:UNUSED_PAD src0_sel:WORD_1 src1_sel:DWORD
	v_and_b32_sdwa v24, v19, v40 dst_sel:DWORD dst_unused:UNUSED_PAD src0_sel:WORD_1 src1_sel:DWORD
	v_add3_u32 v21, v21, v23, s11
	v_add3_u32 v19, v19, v24, s11
	v_and_b32_e32 v21, 0xffff0000, v21
	v_and_b32_e32 v23, 0xffff0000, v19
	v_or_b32_sdwa v19, v21, v20 dst_sel:DWORD dst_unused:UNUSED_PAD src0_sel:DWORD src1_sel:WORD_1
	v_or_b32_sdwa v18, v23, v18 dst_sel:DWORD dst_unused:UNUSED_PAD src0_sel:DWORD src1_sel:WORD_1
	global_store_dwordx2 v[32:33], v[18:19], off offset:1536
	v_mul_f32_e32 v18, v15, v15
	v_mul_f32_e32 v19, v17, v17
	v_fmac_f32_e32 v18, v14, v14
	v_fmac_f32_e32 v19, v16, v16
	v_add_f32_e32 v18, v18, v19
	v_and_b32_sdwa v19, v16, v40 dst_sel:DWORD dst_unused:UNUSED_PAD src0_sel:WORD_1 src1_sel:DWORD
	v_and_b32_sdwa v20, v14, v40 dst_sel:DWORD dst_unused:UNUSED_PAD src0_sel:WORD_1 src1_sel:DWORD
	v_add3_u32 v14, v14, v20, s11
	v_add3_u32 v16, v16, v19, s11
	v_and_b32_sdwa v19, v17, v40 dst_sel:DWORD dst_unused:UNUSED_PAD src0_sel:WORD_1 src1_sel:DWORD
	v_and_b32_sdwa v20, v15, v40 dst_sel:DWORD dst_unused:UNUSED_PAD src0_sel:WORD_1 src1_sel:DWORD
	v_add3_u32 v17, v17, v19, s11
	v_add3_u32 v15, v15, v20, s11
	v_and_b32_e32 v17, 0xffff0000, v17
	v_and_b32_e32 v19, 0xffff0000, v15
	v_or_b32_sdwa v15, v17, v16 dst_sel:DWORD dst_unused:UNUSED_PAD src0_sel:DWORD src1_sel:WORD_1
	v_or_b32_sdwa v14, v19, v14 dst_sel:DWORD dst_unused:UNUSED_PAD src0_sel:DWORD src1_sel:WORD_1
	global_store_dwordx2 v[32:33], v[14:15], off offset:2048
	v_mul_f32_e32 v14, v11, v11
	v_mul_f32_e32 v15, v13, v13
	v_fmac_f32_e32 v14, v10, v10
	v_fmac_f32_e32 v15, v12, v12
	v_add_f32_e32 v14, v14, v15
	v_and_b32_sdwa v15, v12, v40 dst_sel:DWORD dst_unused:UNUSED_PAD src0_sel:WORD_1 src1_sel:DWORD
	v_and_b32_sdwa v16, v10, v40 dst_sel:DWORD dst_unused:UNUSED_PAD src0_sel:WORD_1 src1_sel:DWORD
	v_add3_u32 v10, v10, v16, s11
	v_add3_u32 v12, v12, v15, s11
	v_and_b32_sdwa v15, v13, v40 dst_sel:DWORD dst_unused:UNUSED_PAD src0_sel:WORD_1 src1_sel:DWORD
	v_and_b32_sdwa v16, v11, v40 dst_sel:DWORD dst_unused:UNUSED_PAD src0_sel:WORD_1 src1_sel:DWORD
	v_add3_u32 v13, v13, v15, s11
	v_add3_u32 v11, v11, v16, s11
	v_and_b32_e32 v13, 0xffff0000, v13
	v_and_b32_e32 v15, 0xffff0000, v11
	v_or_b32_sdwa v11, v13, v12 dst_sel:DWORD dst_unused:UNUSED_PAD src0_sel:DWORD src1_sel:WORD_1
	v_or_b32_sdwa v10, v15, v10 dst_sel:DWORD dst_unused:UNUSED_PAD src0_sel:DWORD src1_sel:WORD_1
	v_add_f32_e32 v22, v41, v22
	global_store_dwordx2 v[32:33], v[10:11], off offset:2560
	v_mul_f32_e32 v10, v7, v7
	v_mul_f32_e32 v11, v9, v9
	v_add_f32_e32 v18, v22, v18
	v_fmac_f32_e32 v10, v6, v6
	v_fmac_f32_e32 v11, v8, v8
	v_add_f32_e32 v14, v18, v14
	v_add_f32_e32 v10, v10, v11
	v_add_f32_e32 v10, v14, v10
	v_mul_f32_e32 v13, v3, v3
	v_mul_f32_e32 v14, v5, v5
	v_fmac_f32_e32 v13, v2, v2
	v_fmac_f32_e32 v14, v4, v4
	v_add_f32_e32 v13, v13, v14
	v_add_f32_e32 v10, v10, v13
	v_cndmask_b32_e32 v13, v1, v34, vcc
	v_lshlrev_b32_e32 v13, 2, v13
	ds_bpermute_b32 v13, v13, v10
	v_cmp_lt_i32_e32 vcc, v35, v26
	v_and_b32_sdwa v12, v6, v40 dst_sel:DWORD dst_unused:UNUSED_PAD src0_sel:WORD_1 src1_sel:DWORD
	v_and_b32_sdwa v11, v8, v40 dst_sel:DWORD dst_unused:UNUSED_PAD src0_sel:WORD_1 src1_sel:DWORD
	v_add3_u32 v6, v6, v12, s11
	s_waitcnt lgkmcnt(0)
; __device__ __forceinline__ unsigned pk2(float lo, float hi) { return f2bf(lo) | (f2bf(hi) << 16); }
; __device__ __forceinline__ float wave_sum(float v) {
; #pragma unroll
;     for (int o = 1; o < 64; o <<= 1) v += __shfl_xor(v, o);
;     return v;
; __device__ __forceinline__ void row_item(const float* x, bf16_t* xb, float* ss, int r, int lane) {
;     ...
;     for (int j = 0; j < 16; ++j) { s += (v[j][0] * v[j][0] + v[j][1] * v[j][1]) + (v[j][2] * v[j][2] + v[j][3] * v[j][3]); u32x2 w; w.x = pk2(v[j][0], v[j][1]); w.y = pk2(v[j][2], v[j][3]); o[64 * j] = w; }
;     s = wave_sum(s); if (lane == 0) ss[r] = s;
	v_add_f32_e32 v10, v10, v13
	v_cndmask_b32_e32 v13, v1, v35, vcc
	v_lshlrev_b32_e32 v13, 2, v13
	ds_bpermute_b32 v13, v13, v10
	v_and_b32_sdwa v12, v7, v40 dst_sel:DWORD dst_unused:UNUSED_PAD src0_sel:WORD_1 src1_sel:DWORD
	v_add3_u32 v8, v8, v11, s11
	v_and_b32_sdwa v11, v9, v40 dst_sel:DWORD dst_unused:UNUSED_PAD src0_sel:WORD_1 src1_sel:DWORD
	v_add3_u32 v7, v7, v12, s11
	v_cmp_lt_i32_e32 vcc, v36, v26
	v_add3_u32 v9, v9, v11, s11
	v_and_b32_e32 v11, 0xffff0000, v7
	v_cndmask_b32_e32 v7, v1, v36, vcc
	s_waitcnt lgkmcnt(0)
	v_add_f32_e32 v10, v10, v13
	v_lshlrev_b32_e32 v7, 2, v7
	ds_bpermute_b32 v12, v7, v10
	v_and_b32_e32 v9, 0xffff0000, v9
	v_cmp_lt_i32_e32 vcc, v37, v26
	v_or_b32_sdwa v7, v9, v8 dst_sel:DWORD dst_unused:UNUSED_PAD src0_sel:DWORD src1_sel:WORD_1
	v_or_b32_sdwa v6, v11, v6 dst_sel:DWORD dst_unused:UNUSED_PAD src0_sel:DWORD src1_sel:WORD_1
	v_cndmask_b32_e32 v8, v1, v37, vcc
	global_store_dwordx2 v[32:33], v[6:7], off offset:3072
	s_waitcnt lgkmcnt(0)
	v_add_f32_e32 v7, v10, v12
	v_lshlrev_b32_e32 v8, 2, v8
	ds_bpermute_b32 v8, v8, v7
	v_and_b32_sdwa v6, v4, v40 dst_sel:DWORD dst_unused:UNUSED_PAD src0_sel:WORD_1 src1_sel:DWORD
	v_cmp_lt_i32_e32 vcc, v38, v26
	v_add3_u32 v4, v4, v6, s11
	v_and_b32_sdwa v9, v2, v40 dst_sel:DWORD dst_unused:UNUSED_PAD src0_sel:WORD_1 src1_sel:DWORD
	s_waitcnt lgkmcnt(0)
	v_add_f32_e32 v6, v7, v8
	v_cndmask_b32_e32 v7, v1, v38, vcc
	v_lshlrev_b32_e32 v7, 2, v7
	ds_bpermute_b32 v7, v7, v6
	v_add3_u32 v9, v2, v9, s11
	v_and_b32_sdwa v2, v5, v40 dst_sel:DWORD dst_unused:UNUSED_PAD src0_sel:WORD_1 src1_sel:DWORD
	v_and_b32_sdwa v8, v3, v40 dst_sel:DWORD dst_unused:UNUSED_PAD src0_sel:WORD_1 src1_sel:DWORD
	v_cmp_lt_i32_e32 vcc, v39, v26
	v_add3_u32 v2, v5, v2, s11
	v_add3_u32 v5, v3, v8, s11
	v_cndmask_b32_e32 v3, v1, v39, vcc
	v_and_b32_e32 v8, 0xffff0000, v2
	s_waitcnt lgkmcnt(0)
	v_add_f32_e32 v2, v6, v7
	v_lshlrev_b32_e32 v3, 2, v3
	ds_bpermute_b32 v3, v3, v2
	v_and_b32_e32 v6, 0xffff0000, v5
	v_or_b32_sdwa v5, v8, v4 dst_sel:DWORD dst_unused:UNUSED_PAD src0_sel:DWORD src1_sel:WORD_1
	v_or_b32_sdwa v4, v6, v9 dst_sel:DWORD dst_unused:UNUSED_PAD src0_sel:DWORD src1_sel:WORD_1
	global_store_dwordx2 v[32:33], v[4:5], off offset:3584
	s_and_saveexec_b64 s[6:7], s[4:5]
	s_cbranch_execz .LBB0_54
	s_add_u32 s22, s8, s18
	s_waitcnt lgkmcnt(0)
	v_add_f32_e32 v2, v2, v3
	s_addc_u32 s23, s9, s19
	global_store_dword v27, v2, s[22:23]
	s_branch .LBB0_54
